# C1: attention branch-1 combine (ptrow = g0*ocrow + g1*O) - the 16 row loads issued up front into free VGPR quads and counted down with vmcnt(15) instead of 16 serial load/wait/store round trips; on to
# baseline (speedup 1.0000x reference)
.LBB0_880:
	s_waitcnt vmcnt(0)
	v_add_f32_e32 v0, v160, v164
	v_mul_f32_e32 v0, 0xbfb8aa3b, v0
	v_exp_f32_e32 v0, v0
	s_max_i32 s2, s66, 8
	s_add_i32 s2, s2, -8
	v_readlane_b32 s74, v255, 23
	s_lshl_b64 s[2:3], -1, s2
	v_readlane_b32 s75, v255, 24
	v_add_f32_e32 v0, 1.0, v0
	s_and_b64 s[2:3], s[74:75], s[2:3]
	v_div_scale_f32 v1, s[74:75], v0, v0, 1.0
	v_rcp_f32_e32 v2, v1
	v_lshlrev_b64 v[8:9], 2, v[174:175]
	s_waitcnt vmcnt(0)
	v_fma_f32 v3, -v1, v2, 1.0
	v_fmac_f32_e32 v2, v3, v2
	v_div_scale_f32 v3, vcc, 1.0, v0, 1.0
	v_mul_f32_e32 v4, v3, v2
	v_fma_f32 v5, -v1, v4, v3
	v_fmac_f32_e32 v4, v5, v2
	v_fma_f32 v1, -v1, v4, v3
	v_div_fmas_f32 v1, v1, v2, v4
	v_div_fixup_f32 v4, v1, v0, 1.0
	v_add_f32_e32 v0, v161, v165
	v_mul_f32_e32 v0, 0xbfb8aa3b, v0
	v_exp_f32_e32 v0, v0
	s_barrier
	s_ff1_i32_b64 s94, s[2:3]
	v_add_f32_e32 v0, 1.0, v0
	v_div_scale_f32 v1, s[74:75], v0, v0, 1.0
	v_rcp_f32_e32 v2, v1
	v_readlane_b32 s74, v255, 9
	v_readlane_b32 s75, v255, 10
	s_mul_i32 s67, s94, 0xc8000
	v_fma_f32 v3, -v1, v2, 1.0
	v_fmac_f32_e32 v2, v3, v2
	v_div_scale_f32 v3, vcc, 1.0, v0, 1.0
	v_mul_f32_e32 v5, v3, v2
	v_fma_f32 v6, -v1, v5, v3
	v_fmac_f32_e32 v5, v6, v2
	v_fma_f32 v1, -v1, v5, v3
	v_div_fmas_f32 v1, v1, v2, v5
	v_div_fixup_f32 v6, v1, v0, 1.0
	v_lshlrev_b64 v[0:1], 2, v[184:185]
	v_lshl_add_u64 v[2:3], s[74:75], 0, v[0:1]
	v_readlane_b32 s74, v255, 11
	v_readlane_b32 s75, v255, 12
	v_lshl_add_u64 v[10:11], v[2:3], 0, v[8:9]
	v_readlane_b32 s68, v255, 13
	v_lshl_add_u64 v[0:1], s[74:75], 0, v[0:1]
	v_lshl_add_u64 v[160:161], v[0:1], 0, v[8:9]
	v_mov_b32_e32 v0, v228
	s_nop 1
	v_permlane32_swap_b32_e32 v228, v0
	v_add_f32_e32 v0, v228, v0
	v_div_scale_f32 v1, s[74:75], v0, v0, 1.0
	v_rcp_f32_e32 v2, v1
	s_add_u32 s74, s2, -1
	s_addc_u32 s75, s3, -1
	s_and_b64 s[2:3], s[74:75], s[2:3]
	v_fma_f32 v3, -v1, v2, 1.0
	v_fmac_f32_e32 v2, v3, v2
	v_div_scale_f32 v3, vcc, 1.0, v0, 1.0
	v_mul_f32_e32 v5, v3, v2
	v_fma_f32 v7, -v1, v5, v3
	v_fmac_f32_e32 v5, v7, v2
	v_fma_f32 v1, -v1, v5, v3
	v_div_fmas_f32 v1, v1, v2, v5
	v_div_fixup_f32 v8, v1, v0, 1.0
	global_load_dwordx4 v[64:67], v[10:11], off
	global_load_dwordx4 v[68:71], v[10:11], off offset:32
	global_load_dwordx4 v[72:75], v[10:11], off offset:64
	global_load_dwordx4 v[76:79], v[10:11], off offset:96
	global_load_dwordx4 v[96:99], v[10:11], off offset:128
	global_load_dwordx4 v[100:103], v[10:11], off offset:160
	global_load_dwordx4 v[104:107], v[10:11], off offset:192
	global_load_dwordx4 v[108:111], v[10:11], off offset:224
	global_load_dwordx4 v[112:115], v[10:11], off offset:256
	global_load_dwordx4 v[116:119], v[10:11], off offset:288
	global_load_dwordx4 v[120:123], v[10:11], off offset:320
	global_load_dwordx4 v[124:127], v[10:11], off offset:352
	global_load_dwordx4 v[228:231], v[10:11], off offset:384
	global_load_dwordx4 v[232:235], v[10:11], off offset:416
	global_load_dwordx4 v[236:239], v[10:11], off offset:448
	global_load_dwordx4 v[240:243], v[10:11], off offset:480
	v_pk_mul_f32 v[12:13], v[80:81], v[8:9] op_sel_hi:[1,0]
	s_add_u32 s74, s68, s67
	v_pk_mul_f32 v[12:13], v[6:7], v[12:13] op_sel_hi:[0,1]
	v_readlane_b32 s67, v255, 14
	s_addc_u32 s75, s67, 0
	s_lshl_b32 s67, s94, 7
	v_readlane_b32 s68, v255, 15
	s_add_u32 vcc_lo, s68, s67
	v_readlane_b32 s67, v255, 16
	s_addc_u32 vcc_hi, s67, 0
	s_mov_b32 m0, s69
	v_readlane_b32 s67, v255, 25
	s_cmp_eq_u64 s[2:3], 0
	s_ff1_i32_b64 s84, s[2:3]
	s_waitcnt vmcnt(15)
	v_pk_fma_f32 v[64:65], v[4:5], v[64:65], v[12:13] op_sel_hi:[0,1,1]
	v_pk_mul_f32 v[12:13], v[82:83], v[8:9] op_sel_hi:[1,0]
	s_nop 0
	v_pk_mul_f32 v[12:13], v[6:7], v[12:13] op_sel_hi:[0,1]
	v_pk_fma_f32 v[66:67], v[4:5], v[66:67], v[12:13] op_sel_hi:[0,1,1]
	global_store_dwordx4 v[160:161], v[64:67], off
	v_pk_mul_f32 v[12:13], v[84:85], v[8:9] op_sel_hi:[1,0]
	s_waitcnt vmcnt(15)
	v_pk_mul_f32 v[68:69], v[4:5], v[68:69] op_sel_hi:[0,1]
	v_pk_fma_f32 v[68:69], v[6:7], v[12:13], v[68:69] op_sel_hi:[0,1,1]
	v_pk_mul_f32 v[12:13], v[86:87], v[8:9] op_sel_hi:[1,0]
	v_pk_mul_f32 v[70:71], v[4:5], v[70:71] op_sel_hi:[0,1]
	v_pk_fma_f32 v[70:71], v[6:7], v[12:13], v[70:71] op_sel_hi:[0,1,1]
	global_store_dwordx4 v[160:161], v[68:71], off offset:32
	v_pk_mul_f32 v[12:13], v[88:89], v[8:9] op_sel_hi:[1,0]
	s_waitcnt vmcnt(15)
	v_pk_mul_f32 v[72:73], v[4:5], v[72:73] op_sel_hi:[0,1]
	v_pk_fma_f32 v[72:73], v[6:7], v[12:13], v[72:73] op_sel_hi:[0,1,1]
	v_pk_mul_f32 v[12:13], v[90:91], v[8:9] op_sel_hi:[1,0]
	v_pk_mul_f32 v[74:75], v[4:5], v[74:75] op_sel_hi:[0,1]
	v_pk_fma_f32 v[74:75], v[6:7], v[12:13], v[74:75] op_sel_hi:[0,1,1]
	global_store_dwordx4 v[160:161], v[72:75], off offset:64
	v_pk_mul_f32 v[12:13], v[92:93], v[8:9] op_sel_hi:[1,0]
	s_waitcnt vmcnt(15)
	v_pk_mul_f32 v[76:77], v[4:5], v[76:77] op_sel_hi:[0,1]
	v_pk_fma_f32 v[76:77], v[6:7], v[12:13], v[76:77] op_sel_hi:[0,1,1]
	v_pk_mul_f32 v[12:13], v[94:95], v[8:9] op_sel_hi:[1,0]
	v_pk_mul_f32 v[78:79], v[4:5], v[78:79] op_sel_hi:[0,1]
	v_pk_fma_f32 v[78:79], v[6:7], v[12:13], v[78:79] op_sel_hi:[0,1,1]
	global_store_dwordx4 v[160:161], v[76:79], off offset:96
	v_pk_mul_f32 v[12:13], v[48:49], v[8:9] op_sel_hi:[1,0]
	s_waitcnt vmcnt(15)
	v_pk_mul_f32 v[96:97], v[4:5], v[96:97] op_sel_hi:[0,1]
	v_pk_fma_f32 v[96:97], v[6:7], v[12:13], v[96:97] op_sel_hi:[0,1,1]
	v_pk_mul_f32 v[12:13], v[50:51], v[8:9] op_sel_hi:[1,0]
	v_pk_mul_f32 v[98:99], v[4:5], v[98:99] op_sel_hi:[0,1]
	v_pk_fma_f32 v[98:99], v[6:7], v[12:13], v[98:99] op_sel_hi:[0,1,1]
	global_store_dwordx4 v[160:161], v[96:99], off offset:128
	v_pk_mul_f32 v[12:13], v[52:53], v[8:9] op_sel_hi:[1,0]
	s_waitcnt vmcnt(15)
	v_pk_mul_f32 v[100:101], v[4:5], v[100:101] op_sel_hi:[0,1]
	v_pk_fma_f32 v[100:101], v[6:7], v[12:13], v[100:101] op_sel_hi:[0,1,1]
	v_pk_mul_f32 v[12:13], v[54:55], v[8:9] op_sel_hi:[1,0]
	v_pk_mul_f32 v[102:103], v[4:5], v[102:103] op_sel_hi:[0,1]
	v_pk_fma_f32 v[102:103], v[6:7], v[12:13], v[102:103] op_sel_hi:[0,1,1]
	global_store_dwordx4 v[160:161], v[100:103], off offset:160
	v_pk_mul_f32 v[12:13], v[56:57], v[8:9] op_sel_hi:[1,0]
	s_waitcnt vmcnt(15)
	v_pk_mul_f32 v[104:105], v[4:5], v[104:105] op_sel_hi:[0,1]
	v_pk_fma_f32 v[104:105], v[6:7], v[12:13], v[104:105] op_sel_hi:[0,1,1]
	v_pk_mul_f32 v[12:13], v[58:59], v[8:9] op_sel_hi:[1,0]
	v_pk_mul_f32 v[106:107], v[4:5], v[106:107] op_sel_hi:[0,1]
	v_pk_fma_f32 v[106:107], v[6:7], v[12:13], v[106:107] op_sel_hi:[0,1,1]
	global_store_dwordx4 v[160:161], v[104:107], off offset:192
	v_pk_mul_f32 v[12:13], v[60:61], v[8:9] op_sel_hi:[1,0]
	s_waitcnt vmcnt(15)
	v_pk_mul_f32 v[108:109], v[4:5], v[108:109] op_sel_hi:[0,1]
	v_pk_fma_f32 v[108:109], v[6:7], v[12:13], v[108:109] op_sel_hi:[0,1,1]
	v_pk_mul_f32 v[12:13], v[62:63], v[8:9] op_sel_hi:[1,0]
	v_pk_mul_f32 v[110:111], v[4:5], v[110:111] op_sel_hi:[0,1]
	v_pk_fma_f32 v[110:111], v[6:7], v[12:13], v[110:111] op_sel_hi:[0,1,1]
	global_store_dwordx4 v[160:161], v[108:111], off offset:224
	v_pk_mul_f32 v[12:13], v[32:33], v[8:9] op_sel_hi:[1,0]
	s_waitcnt vmcnt(15)
	v_pk_mul_f32 v[112:113], v[4:5], v[112:113] op_sel_hi:[0,1]
	v_pk_fma_f32 v[112:113], v[6:7], v[12:13], v[112:113] op_sel_hi:[0,1,1]
	v_pk_mul_f32 v[12:13], v[34:35], v[8:9] op_sel_hi:[1,0]
	v_pk_mul_f32 v[114:115], v[4:5], v[114:115] op_sel_hi:[0,1]
	v_pk_fma_f32 v[114:115], v[6:7], v[12:13], v[114:115] op_sel_hi:[0,1,1]
	global_store_dwordx4 v[160:161], v[112:115], off offset:256
	v_pk_mul_f32 v[12:13], v[36:37], v[8:9] op_sel_hi:[1,0]
	s_waitcnt vmcnt(15)
	v_pk_mul_f32 v[116:117], v[4:5], v[116:117] op_sel_hi:[0,1]
	v_pk_fma_f32 v[116:117], v[6:7], v[12:13], v[116:117] op_sel_hi:[0,1,1]
	v_pk_mul_f32 v[12:13], v[38:39], v[8:9] op_sel_hi:[1,0]
	v_pk_mul_f32 v[118:119], v[4:5], v[118:119] op_sel_hi:[0,1]
	v_pk_fma_f32 v[118:119], v[6:7], v[12:13], v[118:119] op_sel_hi:[0,1,1]
	global_store_dwordx4 v[160:161], v[116:119], off offset:288
	v_pk_mul_f32 v[12:13], v[40:41], v[8:9] op_sel_hi:[1,0]
	s_waitcnt vmcnt(15)
	v_pk_mul_f32 v[120:121], v[4:5], v[120:121] op_sel_hi:[0,1]
	v_pk_fma_f32 v[120:121], v[6:7], v[12:13], v[120:121] op_sel_hi:[0,1,1]
	v_pk_mul_f32 v[12:13], v[42:43], v[8:9] op_sel_hi:[1,0]
	v_pk_mul_f32 v[122:123], v[4:5], v[122:123] op_sel_hi:[0,1]
	v_pk_fma_f32 v[122:123], v[6:7], v[12:13], v[122:123] op_sel_hi:[0,1,1]
	global_store_dwordx4 v[160:161], v[120:123], off offset:320
	v_pk_mul_f32 v[12:13], v[44:45], v[8:9] op_sel_hi:[1,0]
	s_waitcnt vmcnt(15)
	v_pk_mul_f32 v[124:125], v[4:5], v[124:125] op_sel_hi:[0,1]
	v_pk_fma_f32 v[124:125], v[6:7], v[12:13], v[124:125] op_sel_hi:[0,1,1]
	v_pk_mul_f32 v[12:13], v[46:47], v[8:9] op_sel_hi:[1,0]
	v_pk_mul_f32 v[126:127], v[4:5], v[126:127] op_sel_hi:[0,1]
	v_pk_fma_f32 v[126:127], v[6:7], v[12:13], v[126:127] op_sel_hi:[0,1,1]
	global_store_dwordx4 v[160:161], v[124:127], off offset:352
	v_pk_mul_f32 v[12:13], v[16:17], v[8:9] op_sel_hi:[1,0]
	s_waitcnt vmcnt(15)
	v_pk_mul_f32 v[228:229], v[4:5], v[228:229] op_sel_hi:[0,1]
	v_pk_fma_f32 v[228:229], v[6:7], v[12:13], v[228:229] op_sel_hi:[0,1,1]
	v_pk_mul_f32 v[12:13], v[18:19], v[8:9] op_sel_hi:[1,0]
	v_pk_mul_f32 v[230:231], v[4:5], v[230:231] op_sel_hi:[0,1]
	v_pk_fma_f32 v[230:231], v[6:7], v[12:13], v[230:231] op_sel_hi:[0,1,1]
	global_store_dwordx4 v[160:161], v[228:231], off offset:384
	v_pk_mul_f32 v[12:13], v[20:21], v[8:9] op_sel_hi:[1,0]
	s_waitcnt vmcnt(15)
	v_pk_mul_f32 v[232:233], v[4:5], v[232:233] op_sel_hi:[0,1]
	v_pk_fma_f32 v[232:233], v[6:7], v[12:13], v[232:233] op_sel_hi:[0,1,1]
	v_pk_mul_f32 v[12:13], v[22:23], v[8:9] op_sel_hi:[1,0]
	v_pk_mul_f32 v[234:235], v[4:5], v[234:235] op_sel_hi:[0,1]
	v_pk_fma_f32 v[234:235], v[6:7], v[12:13], v[234:235] op_sel_hi:[0,1,1]
	global_store_dwordx4 v[160:161], v[232:235], off offset:416
	v_pk_mul_f32 v[12:13], v[24:25], v[8:9] op_sel_hi:[1,0]
	s_waitcnt vmcnt(15)
	v_pk_mul_f32 v[236:237], v[4:5], v[236:237] op_sel_hi:[0,1]
	v_pk_fma_f32 v[236:237], v[6:7], v[12:13], v[236:237] op_sel_hi:[0,1,1]
	v_pk_mul_f32 v[12:13], v[26:27], v[8:9] op_sel_hi:[1,0]
	v_pk_mul_f32 v[238:239], v[4:5], v[238:239] op_sel_hi:[0,1]
	v_pk_fma_f32 v[238:239], v[6:7], v[12:13], v[238:239] op_sel_hi:[0,1,1]
	global_store_dwordx4 v[160:161], v[236:239], off offset:448
	v_pk_mul_f32 v[12:13], v[28:29], v[8:9] op_sel_hi:[1,0]
	v_pk_mul_f32 v[8:9], v[30:31], v[8:9] op_sel_hi:[1,0]
	s_waitcnt vmcnt(15)
	v_pk_mul_f32 v[240:241], v[4:5], v[240:241] op_sel_hi:[0,1]
	v_pk_mul_f32 v[242:243], v[4:5], v[242:243] op_sel_hi:[0,1]
	v_pk_fma_f32 v[240:241], v[6:7], v[12:13], v[240:241] op_sel_hi:[0,1,1]
	v_pk_fma_f32 v[242:243], v[6:7], v[8:9], v[242:243] op_sel_hi:[0,1,1]
	global_store_dwordx4 v[160:161], v[240:243], off offset:480
	s_waitcnt vmcnt(0)
	s_nop 1
	v_lshl_add_u64 v[0:1], s[74:75], 0, v[168:169]
	global_load_lds_dwordx4 v[0:1], off
	v_lshl_add_u64 v[0:1], vcc, 0, v[176:177]
	s_mov_b32 m0, s67
	v_readlane_b32 s67, v255, 26
	global_load_lds_dwordx4 v[0:1], off
	v_lshl_add_u64 v[0:1], s[74:75], 0, v[178:179]
	s_mov_b32 m0, s67
	v_readlane_b32 s67, v255, 27
	global_load_lds_dwordx4 v[0:1], off
	v_lshl_add_u64 v[0:1], vcc, 0, v[180:181]
	s_mov_b32 m0, s67
	s_cselect_b64 s[74:75], -1, 0
	global_load_lds_dwordx4 v[0:1], off
	s_and_b64 vcc, exec, s[74:75]
	s_cbranch_vccnz .LBB0_882
	s_mul_i32 s67, s84, 0xc8000
	v_readlane_b32 s68, v255, 13
	s_add_u32 s78, s68, s67
	v_readlane_b32 s67, v255, 14
	s_addc_u32 s79, s67, 0
	s_lshl_b64 s[80:81], s[84:85], 7
	v_readlane_b32 s67, v255, 15
	s_add_u32 s80, s67, s80
	v_readlane_b32 s67, v255, 16
	s_addc_u32 s81, s67, s81
	v_lshl_add_u64 v[0:1], s[78:79], 0, v[168:169]
	s_add_i32 m0, s69, 0x8000
	v_readlane_b32 s67, v254, 57
	global_load_lds_dwordx4 v[0:1], off
	v_lshl_add_u64 v[0:1], s[80:81], 0, v[176:177]
	s_add_i32 m0, s69, 0xc000
	s_nop 0
	global_load_lds_dwordx4 v[0:1], off
	v_lshl_add_u64 v[0:1], s[78:79], 0, v[178:179]
	s_mov_b32 m0, s67
	v_readlane_b32 s67, v254, 58
	global_load_lds_dwordx4 v[0:1], off
	v_lshl_add_u64 v[0:1], s[80:81], 0, v[180:181]
	s_mov_b32 m0, s67
	s_nop 0
	global_load_lds_dwordx4 v[0:1], off
